# v43 + GEMM1 SwiGLU epilogue: store address as one 32-bit v_lshl_add_u32 against a per-unit base with SGPR base in the store (was five 64-bit ops per block), zero fills before the fp8 convert pairs rem
# speedup vs baseline: 1.0024x; 1.0024x over previous
; __device__ __forceinline__ float fast_exp2(float x) { return __builtin_amdgcn_exp2f(x); }
; __device__ __forceinline__ float fast_rcp(float x) { return __builtin_amdgcn_rcpf(x); }
;     __device__ __forceinline__ void operator()(const f32x4 (&acc)[2][2][4][2], const Unit& u, int wr, int wc, int fr, int fq) const {
;         const int col0 = u.nt * 128 + wc * 32 + 8 * fq;
; #pragma unroll
;         for (int ai = 0; ai < 2; ++ai)
; #pragma unroll
;             for (int m = 0; m < 4; ++m) { const int rl = ai * 128 + wr * 64 + m * 16 + fr;
;                 f32x4 ov[2];
; #pragma unroll
;                 for (int n = 0; n < 2; ++n) { const f32x4 g = acc[ai][0][m][n], gu = g * acc[ai][1][m][n];
;                     f32x4 d; d.x = fast_exp2(g.x); d.y = fast_exp2(g.y); d.z = fast_exp2(g.z); d.w = fast_exp2(g.w);
;                     d = d + 1.f;
;                     f32x4 r; r.x = fast_rcp(d.x); r.y = fast_rcp(d.y); r.z = fast_rcp(d.z); r.w = fast_rcp(d.w);
;                     ov[n] = gu * r; }
; #pragma unroll
;                 for (int j = 0; j < 4; ++j) { ov[0][j] = __builtin_amdgcn_fmed3f(ov[0][j], -448.f, 448.f); ov[1][j] = __builtin_amdgcn_fmed3f(ov[1][j], -448.f, 448.f); }
;                 int w0 = __builtin_amdgcn_cvt_pk_fp8_f32(ov[0].x, ov[0].y, 0, false); w0 = __builtin_amdgcn_cvt_pk_fp8_f32(ov[0].z, ov[0].w, w0, true);
;                 int w1 = __builtin_amdgcn_cvt_pk_fp8_f32(ov[1].x, ov[1].y, 0, false); w1 = __builtin_amdgcn_cvt_pk_fp8_f32(ov[1].z, ov[1].w, w1, true);
;                 u32x2 w; w.x = (unsigned)w0; w.y = (unsigned)w1;
;                 if (rl < u.nv) *(u32x2*)(act + (size_t)(u.row0 + rl) * EDIM + col0) = w; }
.LBB0_741:
	s_nop 15
	s_nop 15
	v_lshl_or_b32 v2, s70, 7, v231
	v_ashrrev_i32_e32 v3, 31, v2
	v_lshl_add_u32 v16, s37, 8, v2
	v_cmp_gt_i32_e32 vcc, s43, v207
	s_and_saveexec_b64 s[4:5], vcc
	s_cbranch_execnz .LBB0_750
	s_or_b64 exec, exec, s[4:5]
	v_cmp_gt_i32_e32 vcc, s43, v224
	s_and_saveexec_b64 s[4:5], vcc
	s_cbranch_execnz .LBB0_751

; __device__ __forceinline__ float fast_exp2(float x) { return __builtin_amdgcn_exp2f(x); }
; __device__ __forceinline__ float fast_rcp(float x) { return __builtin_amdgcn_rcpf(x); }
;     __device__ __forceinline__ void operator()(const f32x4 (&acc)[2][2][4][2], const Unit& u, int wr, int wc, int fr, int fq) const {
;     ...
;             for (int m = 0; m < 4; ++m) { const int rl = ai * 128 + wr * 64 + m * 16 + fr;
;                 f32x4 ov[2];
; #pragma unroll
;                 for (int n = 0; n < 2; ++n) { const f32x4 g = acc[ai][0][m][n], gu = g * acc[ai][1][m][n];
;                     f32x4 d; d.x = fast_exp2(g.x); d.y = fast_exp2(g.y); d.z = fast_exp2(g.z); d.w = fast_exp2(g.w);
;                     d = d + 1.f;
;                     f32x4 r; r.x = fast_rcp(d.x); r.y = fast_rcp(d.y); r.z = fast_rcp(d.z); r.w = fast_rcp(d.w);
;                     ov[n] = gu * r; }
; #pragma unroll
;                 for (int j = 0; j < 4; ++j) { ov[0][j] = __builtin_amdgcn_fmed3f(ov[0][j], -448.f, 448.f); ov[1][j] = __builtin_amdgcn_fmed3f(ov[1][j], -448.f, 448.f); }
;                 int w0 = __builtin_amdgcn_cvt_pk_fp8_f32(ov[0].x, ov[0].y, 0, false); w0 = __builtin_amdgcn_cvt_pk_fp8_f32(ov[0].z, ov[0].w, w0, true);
;                 int w1 = __builtin_amdgcn_cvt_pk_fp8_f32(ov[1].x, ov[1].y, 0, false); w1 = __builtin_amdgcn_cvt_pk_fp8_f32(ov[1].z, ov[1].w, w1, true);
;                 u32x2 w; w.x = (unsigned)w0; w.y = (unsigned)w1;
;                 if (rl < u.nv) *(u32x2*)(act + (size_t)(u.row0 + rl) * EDIM + col0) = w; }
.LBB0_750:
	v_exp_f32_e32 v6, v196
	v_exp_f32_e32 v7, v197
	v_exp_f32_e32 v10, v194
	v_exp_f32_e32 v11, v195
	v_pk_mul_f32 v[4:5], v[196:197], v[192:193]
	v_pk_add_f32 v[6:7], v[6:7], 1.0 op_sel_hi:[1,0]
	v_exp_f32_e32 v12, v188
	v_rcp_f32_e32 v6, v6
	v_rcp_f32_e32 v7, v7
	v_pk_add_f32 v[10:11], v[10:11], 1.0 op_sel_hi:[1,0]
	v_exp_f32_e32 v13, v189
	v_rcp_f32_e32 v10, v10
	v_pk_mul_f32 v[4:5], v[4:5], v[6:7]
	v_exp_f32_e32 v6, v186
	v_exp_f32_e32 v7, v187
	v_rcp_f32_e32 v11, v11
	v_pk_mul_f32 v[8:9], v[194:195], v[190:191]
	v_pk_mul_f32 v[14:15], v[186:187], v[182:183]
	v_pk_add_f32 v[6:7], v[6:7], 1.0 op_sel_hi:[1,0]
	v_pk_mul_f32 v[8:9], v[8:9], v[10:11]
	v_pk_add_f32 v[10:11], v[12:13], 1.0 op_sel_hi:[1,0]
	v_rcp_f32_e32 v6, v6
	v_rcp_f32_e32 v7, v7
	v_rcp_f32_e32 v10, v10
	v_rcp_f32_e32 v11, v11
	v_pk_mul_f32 v[12:13], v[188:189], v[184:185]
	v_pk_mul_f32 v[6:7], v[14:15], v[6:7]
	v_med3_f32 v9, v9, s52, v235
	v_pk_mul_f32 v[10:11], v[12:13], v[10:11]
	v_med3_f32 v7, v7, s52, v235
	v_med3_f32 v12, v6, s52, v235
	v_med3_f32 v8, v8, s52, v235
	v_cvt_pk_fp8_f32 v6, v12, v7
	v_cvt_pk_fp8_f32 v7, v8, v9
	v_med3_f32 v5, v5, s52, v235
	v_med3_f32 v4, v4, s52, v235
	v_med3_f32 v11, v11, s52, v235
	v_med3_f32 v8, v10, s52, v235
	v_cvt_pk_fp8_f32 v7, v4, v5 op_sel:[0,0,1]
	v_lshl_add_u32 v4, v207, 8, v16
	v_cvt_pk_fp8_f32 v6, v8, v11 op_sel:[0,0,1]
	global_store_dwordx2 v4, v[6:7], s[12:13]
	s_or_b64 exec, exec, s[4:5]
	v_cmp_gt_i32_e32 vcc, s43, v224
	s_and_saveexec_b64 s[4:5], vcc
	s_cbranch_execz .LBB0_743
.LBB0_751:
	v_exp_f32_e32 v6, v180
	v_exp_f32_e32 v7, v181
	v_exp_f32_e32 v10, v178
	v_exp_f32_e32 v11, v179
	v_pk_mul_f32 v[4:5], v[180:181], v[176:177]
	v_pk_add_f32 v[6:7], v[6:7], 1.0 op_sel_hi:[1,0]
	v_exp_f32_e32 v12, v172
	v_rcp_f32_e32 v6, v6
	v_rcp_f32_e32 v7, v7
	v_pk_add_f32 v[10:11], v[10:11], 1.0 op_sel_hi:[1,0]
	v_exp_f32_e32 v13, v173
	v_rcp_f32_e32 v10, v10
	v_pk_mul_f32 v[4:5], v[4:5], v[6:7]
	v_exp_f32_e32 v6, v170
	v_exp_f32_e32 v7, v171
	v_rcp_f32_e32 v11, v11
	v_pk_mul_f32 v[8:9], v[178:179], v[174:175]
	v_pk_mul_f32 v[14:15], v[170:171], v[166:167]
	v_pk_add_f32 v[6:7], v[6:7], 1.0 op_sel_hi:[1,0]
	v_pk_mul_f32 v[8:9], v[8:9], v[10:11]
	v_pk_add_f32 v[10:11], v[12:13], 1.0 op_sel_hi:[1,0]
	v_rcp_f32_e32 v6, v6
	v_rcp_f32_e32 v7, v7
	v_rcp_f32_e32 v10, v10
	v_rcp_f32_e32 v11, v11
	v_pk_mul_f32 v[12:13], v[172:173], v[168:169]
	v_pk_mul_f32 v[6:7], v[14:15], v[6:7]
	v_med3_f32 v9, v9, s52, v235
	v_pk_mul_f32 v[10:11], v[12:13], v[10:11]
	v_med3_f32 v7, v7, s52, v235
	v_med3_f32 v12, v6, s52, v235
	v_med3_f32 v8, v8, s52, v235
	v_cvt_pk_fp8_f32 v6, v12, v7
	v_cvt_pk_fp8_f32 v7, v8, v9
	v_med3_f32 v5, v5, s52, v235
	v_med3_f32 v4, v4, s52, v235
	v_med3_f32 v11, v11, s52, v235
	v_med3_f32 v8, v10, s52, v235
	v_cvt_pk_fp8_f32 v7, v4, v5 op_sel:[0,0,1]
	v_lshl_add_u32 v4, v224, 8, v16
	v_cvt_pk_fp8_f32 v6, v8, v11 op_sel:[0,0,1]
	global_store_dwordx2 v4, v[6:7], s[12:13]
	s_or_b64 exec, exec, s[4:5]
	v_cmp_gt_i32_e32 vcc, s43, v225
	s_and_saveexec_b64 s[4:5], vcc
	s_cbranch_execz .LBB0_744
.LBB0_752:
	v_exp_f32_e32 v6, v164
	v_exp_f32_e32 v7, v165
	v_exp_f32_e32 v10, v162
	v_exp_f32_e32 v11, v163
	v_pk_mul_f32 v[4:5], v[164:165], v[160:161]
	v_pk_add_f32 v[6:7], v[6:7], 1.0 op_sel_hi:[1,0]
	v_exp_f32_e32 v12, v156
	v_rcp_f32_e32 v6, v6
	v_rcp_f32_e32 v7, v7
	v_pk_add_f32 v[10:11], v[10:11], 1.0 op_sel_hi:[1,0]
	v_exp_f32_e32 v13, v157
	v_rcp_f32_e32 v10, v10
	v_pk_mul_f32 v[4:5], v[4:5], v[6:7]
	v_exp_f32_e32 v6, v154
	v_exp_f32_e32 v7, v155
	v_rcp_f32_e32 v11, v11
	v_pk_mul_f32 v[8:9], v[162:163], v[158:159]
	v_pk_mul_f32 v[14:15], v[154:155], v[150:151]
	v_pk_add_f32 v[6:7], v[6:7], 1.0 op_sel_hi:[1,0]
	v_pk_mul_f32 v[8:9], v[8:9], v[10:11]
	v_pk_add_f32 v[10:11], v[12:13], 1.0 op_sel_hi:[1,0]
	v_rcp_f32_e32 v6, v6
	v_rcp_f32_e32 v7, v7
	v_rcp_f32_e32 v10, v10
	v_rcp_f32_e32 v11, v11
	v_pk_mul_f32 v[12:13], v[156:157], v[152:153]
	v_pk_mul_f32 v[6:7], v[14:15], v[6:7]
	v_med3_f32 v9, v9, s52, v235
	v_pk_mul_f32 v[10:11], v[12:13], v[10:11]
	v_med3_f32 v7, v7, s52, v235
	v_med3_f32 v12, v6, s52, v235
	v_med3_f32 v8, v8, s52, v235
	v_cvt_pk_fp8_f32 v6, v12, v7
	v_cvt_pk_fp8_f32 v7, v8, v9
	v_med3_f32 v5, v5, s52, v235
	v_med3_f32 v4, v4, s52, v235
	v_med3_f32 v11, v11, s52, v235
	v_med3_f32 v8, v10, s52, v235
	v_cvt_pk_fp8_f32 v7, v4, v5 op_sel:[0,0,1]
	v_lshl_add_u32 v4, v225, 8, v16
	v_cvt_pk_fp8_f32 v6, v8, v11 op_sel:[0,0,1]
	global_store_dwordx2 v4, v[6:7], s[12:13]
	s_or_b64 exec, exec, s[4:5]
	v_cmp_gt_i32_e32 vcc, s43, v226
	s_and_saveexec_b64 s[4:5], vcc
	s_cbranch_execz .LBB0_745
.LBB0_753:
	v_exp_f32_e32 v6, v148
	v_exp_f32_e32 v7, v149
	v_exp_f32_e32 v10, v146
	v_exp_f32_e32 v11, v147
	v_pk_mul_f32 v[4:5], v[148:149], v[140:141]
	v_pk_add_f32 v[6:7], v[6:7], 1.0 op_sel_hi:[1,0]
	v_exp_f32_e32 v12, v144
	v_rcp_f32_e32 v6, v6
	v_rcp_f32_e32 v7, v7
	v_pk_add_f32 v[10:11], v[10:11], 1.0 op_sel_hi:[1,0]
	v_exp_f32_e32 v13, v145
	v_rcp_f32_e32 v10, v10
	v_pk_mul_f32 v[4:5], v[4:5], v[6:7]
	v_exp_f32_e32 v6, v142
	v_exp_f32_e32 v7, v143
	v_rcp_f32_e32 v11, v11
	v_pk_mul_f32 v[8:9], v[146:147], v[138:139]
	v_pk_mul_f32 v[14:15], v[142:143], v[134:135]
	v_pk_add_f32 v[6:7], v[6:7], 1.0 op_sel_hi:[1,0]
	v_pk_mul_f32 v[8:9], v[8:9], v[10:11]
	v_pk_add_f32 v[10:11], v[12:13], 1.0 op_sel_hi:[1,0]
	v_rcp_f32_e32 v6, v6
	v_rcp_f32_e32 v7, v7
	v_rcp_f32_e32 v10, v10
	v_rcp_f32_e32 v11, v11
	v_pk_mul_f32 v[12:13], v[144:145], v[136:137]
	v_pk_mul_f32 v[6:7], v[14:15], v[6:7]
	v_med3_f32 v9, v9, s52, v235
	v_pk_mul_f32 v[10:11], v[12:13], v[10:11]
	v_med3_f32 v7, v7, s52, v235
	v_med3_f32 v12, v6, s52, v235
	v_med3_f32 v8, v8, s52, v235
	v_cvt_pk_fp8_f32 v6, v12, v7
	v_cvt_pk_fp8_f32 v7, v8, v9
	v_med3_f32 v5, v5, s52, v235
	v_med3_f32 v4, v4, s52, v235
	v_med3_f32 v11, v11, s52, v235
	v_med3_f32 v8, v10, s52, v235
	v_cvt_pk_fp8_f32 v7, v4, v5 op_sel:[0,0,1]
	v_lshl_add_u32 v4, v226, 8, v16
	v_cvt_pk_fp8_f32 v6, v8, v11 op_sel:[0,0,1]
	global_store_dwordx2 v4, v[6:7], s[12:13]
	s_or_b64 exec, exec, s[4:5]
	v_cmp_gt_i32_e32 vcc, s43, v227
	s_and_saveexec_b64 s[4:5], vcc
	s_cbranch_execz .LBB0_746
; __device__ __forceinline__ float fast_exp2(float x) { return __builtin_amdgcn_exp2f(x); }
; __device__ __forceinline__ float fast_rcp(float x) { return __builtin_amdgcn_rcpf(x); }
;     __device__ __forceinline__ void operator()(const f32x4 (&acc)[2][2][4][2], const Unit& u, int wr, int wc, int fr, int fq) const {
;     ...
;             for (int m = 0; m < 4; ++m) { const int rl = ai * 128 + wr * 64 + m * 16 + fr;
;                 f32x4 ov[2];
; #pragma unroll
;                 for (int n = 0; n < 2; ++n) { const f32x4 g = acc[ai][0][m][n], gu = g * acc[ai][1][m][n];
;                     f32x4 d; d.x = fast_exp2(g.x); d.y = fast_exp2(g.y); d.z = fast_exp2(g.z); d.w = fast_exp2(g.w);
;                     d = d + 1.f;
;                     f32x4 r; r.x = fast_rcp(d.x); r.y = fast_rcp(d.y); r.z = fast_rcp(d.z); r.w = fast_rcp(d.w);
;                     ov[n] = gu * r; }
; #pragma unroll
;                 for (int j = 0; j < 4; ++j) { ov[0][j] = __builtin_amdgcn_fmed3f(ov[0][j], -448.f, 448.f); ov[1][j] = __builtin_amdgcn_fmed3f(ov[1][j], -448.f, 448.f); }
;                 int w0 = __builtin_amdgcn_cvt_pk_fp8_f32(ov[0].x, ov[0].y, 0, false); w0 = __builtin_amdgcn_cvt_pk_fp8_f32(ov[0].z, ov[0].w, w0, true);
;                 int w1 = __builtin_amdgcn_cvt_pk_fp8_f32(ov[1].x, ov[1].y, 0, false); w1 = __builtin_amdgcn_cvt_pk_fp8_f32(ov[1].z, ov[1].w, w1, true);
;                 u32x2 w; w.x = (unsigned)w0; w.y = (unsigned)w1;
;                 if (rl < u.nv) *(u32x2*)(act + (size_t)(u.row0 + rl) * EDIM + col0) = w; }
.LBB0_754:
	v_exp_f32_e32 v6, v132
	v_exp_f32_e32 v7, v133
	v_exp_f32_e32 v10, v130
	v_exp_f32_e32 v11, v131
	v_pk_mul_f32 v[4:5], v[128:129], v[132:133]
	v_pk_add_f32 v[6:7], v[6:7], 1.0 op_sel_hi:[1,0]
	v_exp_f32_e32 v12, v124
	v_rcp_f32_e32 v6, v6
	v_rcp_f32_e32 v7, v7
	v_pk_add_f32 v[10:11], v[10:11], 1.0 op_sel_hi:[1,0]
	v_exp_f32_e32 v13, v125
	v_rcp_f32_e32 v10, v10
	v_pk_mul_f32 v[4:5], v[4:5], v[6:7]
	v_exp_f32_e32 v6, v122
	v_exp_f32_e32 v7, v123
	v_rcp_f32_e32 v11, v11
	v_pk_mul_f32 v[8:9], v[126:127], v[130:131]
	v_pk_mul_f32 v[14:15], v[118:119], v[122:123]
	v_pk_add_f32 v[6:7], v[6:7], 1.0 op_sel_hi:[1,0]
	v_pk_mul_f32 v[8:9], v[8:9], v[10:11]
	v_pk_add_f32 v[10:11], v[12:13], 1.0 op_sel_hi:[1,0]
	v_rcp_f32_e32 v6, v6
	v_rcp_f32_e32 v7, v7
	v_rcp_f32_e32 v10, v10
	v_rcp_f32_e32 v11, v11
	v_pk_mul_f32 v[12:13], v[120:121], v[124:125]
	v_pk_mul_f32 v[6:7], v[14:15], v[6:7]
	v_med3_f32 v9, v9, s52, v235
	v_pk_mul_f32 v[10:11], v[12:13], v[10:11]
	v_med3_f32 v7, v7, s52, v235
	v_med3_f32 v12, v6, s52, v235
	v_med3_f32 v8, v8, s52, v235
	v_cvt_pk_fp8_f32 v6, v12, v7
	v_cvt_pk_fp8_f32 v7, v8, v9
	v_med3_f32 v5, v5, s52, v235
	v_med3_f32 v4, v4, s52, v235
	v_med3_f32 v11, v11, s52, v235
	v_med3_f32 v8, v10, s52, v235
	v_cvt_pk_fp8_f32 v7, v4, v5 op_sel:[0,0,1]
	v_lshl_add_u32 v4, v227, 8, v16
	v_cvt_pk_fp8_f32 v6, v8, v11 op_sel:[0,0,1]
	global_store_dwordx2 v4, v[6:7], s[12:13]
	s_or_b64 exec, exec, s[4:5]
	v_cmp_gt_i32_e32 vcc, s43, v228
	s_and_saveexec_b64 s[4:5], vcc
	s_cbranch_execz .LBB0_747
.LBB0_755:
	v_exp_f32_e32 v6, v116
	v_exp_f32_e32 v7, v117
	v_exp_f32_e32 v10, v114
	v_exp_f32_e32 v11, v115
	v_pk_mul_f32 v[4:5], v[112:113], v[116:117]
	v_pk_add_f32 v[6:7], v[6:7], 1.0 op_sel_hi:[1,0]
	v_exp_f32_e32 v12, v108
	v_rcp_f32_e32 v6, v6
	v_rcp_f32_e32 v7, v7
	v_pk_add_f32 v[10:11], v[10:11], 1.0 op_sel_hi:[1,0]
	v_exp_f32_e32 v13, v109
	v_rcp_f32_e32 v10, v10
	v_pk_mul_f32 v[4:5], v[4:5], v[6:7]
	v_exp_f32_e32 v6, v106
	v_exp_f32_e32 v7, v107
	v_rcp_f32_e32 v11, v11
	v_pk_mul_f32 v[8:9], v[110:111], v[114:115]
	v_pk_mul_f32 v[14:15], v[102:103], v[106:107]
	v_pk_add_f32 v[6:7], v[6:7], 1.0 op_sel_hi:[1,0]
	v_pk_mul_f32 v[8:9], v[8:9], v[10:11]
	v_pk_add_f32 v[10:11], v[12:13], 1.0 op_sel_hi:[1,0]
	v_rcp_f32_e32 v6, v6
	v_rcp_f32_e32 v7, v7
	v_rcp_f32_e32 v10, v10
	v_rcp_f32_e32 v11, v11
	v_pk_mul_f32 v[12:13], v[104:105], v[108:109]
	v_pk_mul_f32 v[6:7], v[14:15], v[6:7]
	v_med3_f32 v9, v9, s52, v235
	v_pk_mul_f32 v[10:11], v[12:13], v[10:11]
	v_med3_f32 v7, v7, s52, v235
	v_med3_f32 v12, v6, s52, v235
	v_med3_f32 v8, v8, s52, v235
	v_cvt_pk_fp8_f32 v6, v12, v7
	v_cvt_pk_fp8_f32 v7, v8, v9
	v_med3_f32 v5, v5, s52, v235
	v_med3_f32 v4, v4, s52, v235
	v_med3_f32 v11, v11, s52, v235
	v_med3_f32 v8, v10, s52, v235
	v_cvt_pk_fp8_f32 v7, v4, v5 op_sel:[0,0,1]
	v_lshl_add_u32 v4, v228, 8, v16
	v_cvt_pk_fp8_f32 v6, v8, v11 op_sel:[0,0,1]
	global_store_dwordx2 v4, v[6:7], s[12:13]
	s_or_b64 exec, exec, s[4:5]
	v_cmp_gt_i32_e32 vcc, s43, v229
	s_and_saveexec_b64 s[4:5], vcc
	s_cbranch_execz .LBB0_748
.LBB0_756:
	v_exp_f32_e32 v6, v96
	v_exp_f32_e32 v7, v97
	v_exp_f32_e32 v10, v94
	v_exp_f32_e32 v11, v95
	v_pk_mul_f32 v[4:5], v[96:97], v[100:101]
	v_pk_add_f32 v[6:7], v[6:7], 1.0 op_sel_hi:[1,0]
	v_exp_f32_e32 v12, v88
	v_rcp_f32_e32 v6, v6
	v_rcp_f32_e32 v7, v7
	v_pk_add_f32 v[10:11], v[10:11], 1.0 op_sel_hi:[1,0]
	v_exp_f32_e32 v13, v89
	v_rcp_f32_e32 v10, v10
	v_pk_mul_f32 v[4:5], v[4:5], v[6:7]
	v_exp_f32_e32 v6, v86
	v_exp_f32_e32 v7, v87
	v_rcp_f32_e32 v11, v11
	v_pk_mul_f32 v[8:9], v[94:95], v[98:99]
	v_pk_mul_f32 v[14:15], v[86:87], v[90:91]
	v_pk_add_f32 v[6:7], v[6:7], 1.0 op_sel_hi:[1,0]
	v_pk_mul_f32 v[8:9], v[8:9], v[10:11]
	v_pk_add_f32 v[10:11], v[12:13], 1.0 op_sel_hi:[1,0]
	v_rcp_f32_e32 v6, v6
	v_rcp_f32_e32 v7, v7
	v_rcp_f32_e32 v10, v10
	v_rcp_f32_e32 v11, v11
	v_pk_mul_f32 v[12:13], v[88:89], v[92:93]
	v_pk_mul_f32 v[6:7], v[14:15], v[6:7]
	v_med3_f32 v9, v9, s52, v235
	v_pk_mul_f32 v[10:11], v[12:13], v[10:11]
	v_med3_f32 v7, v7, s52, v235
	v_med3_f32 v12, v6, s52, v235
	v_med3_f32 v8, v8, s52, v235
	v_cvt_pk_fp8_f32 v6, v12, v7
	v_cvt_pk_fp8_f32 v7, v8, v9
	v_med3_f32 v5, v5, s52, v235
	v_med3_f32 v4, v4, s52, v235
	v_med3_f32 v11, v11, s52, v235
	v_med3_f32 v8, v10, s52, v235
	v_cvt_pk_fp8_f32 v7, v4, v5 op_sel:[0,0,1]
	v_lshl_add_u32 v4, v229, 8, v16
	v_cvt_pk_fp8_f32 v6, v8, v11 op_sel:[0,0,1]
	global_store_dwordx2 v4, v[6:7], s[12:13]
	s_or_b64 exec, exec, s[4:5]
	v_cmp_gt_i32_e32 vcc, s43, v230
	s_and_saveexec_b64 s[4:5], vcc
	s_cbranch_execz .LBB0_749
.LBB0_757:
	v_exp_f32_e32 v6, v80
	v_exp_f32_e32 v7, v81
	v_exp_f32_e32 v10, v78
	v_exp_f32_e32 v11, v79
	v_pk_mul_f32 v[4:5], v[80:81], v[84:85]
	v_pk_add_f32 v[6:7], v[6:7], 1.0 op_sel_hi:[1,0]
	v_exp_f32_e32 v12, v72
	v_rcp_f32_e32 v6, v6
	v_rcp_f32_e32 v7, v7
	v_pk_add_f32 v[10:11], v[10:11], 1.0 op_sel_hi:[1,0]
	v_exp_f32_e32 v13, v73
	v_rcp_f32_e32 v10, v10
	v_pk_mul_f32 v[4:5], v[4:5], v[6:7]
	v_exp_f32_e32 v6, v70
	v_exp_f32_e32 v7, v71
	v_rcp_f32_e32 v11, v11
	v_pk_mul_f32 v[8:9], v[78:79], v[82:83]
	v_pk_mul_f32 v[14:15], v[70:71], v[74:75]
	v_pk_add_f32 v[6:7], v[6:7], 1.0 op_sel_hi:[1,0]
	v_pk_mul_f32 v[8:9], v[8:9], v[10:11]
	v_pk_add_f32 v[10:11], v[12:13], 1.0 op_sel_hi:[1,0]
	v_rcp_f32_e32 v6, v6
	v_rcp_f32_e32 v7, v7
	v_rcp_f32_e32 v10, v10
	v_rcp_f32_e32 v11, v11
	v_pk_mul_f32 v[12:13], v[72:73], v[76:77]
	v_pk_mul_f32 v[6:7], v[14:15], v[6:7]
	v_med3_f32 v9, v9, s52, v235
	v_pk_mul_f32 v[10:11], v[12:13], v[10:11]
	v_med3_f32 v7, v7, s52, v235
	v_med3_f32 v12, v6, s52, v235
	v_med3_f32 v8, v8, s52, v235
	v_cvt_pk_fp8_f32 v6, v12, v7
	v_cvt_pk_fp8_f32 v7, v8, v9
	v_med3_f32 v5, v5, s52, v235
	v_med3_f32 v4, v4, s52, v235
	v_med3_f32 v11, v11, s52, v235
	v_med3_f32 v8, v10, s52, v235
	v_cvt_pk_fp8_f32 v7, v4, v5 op_sel:[0,0,1]
	v_lshl_add_u32 v4, v230, 8, v16
	v_cvt_pk_fp8_f32 v6, v8, v11 op_sel:[0,0,1]
	global_store_dwordx2 v4, v[6:7], s[12:13]
	s_or_b64 exec, exec, s[4:5]
	s_cmp_eq_u32 s48, s51
	s_mov_b64 s[4:5], -1
	s_cbranch_scc1 .LBB0_728

;     __device__ __forceinline__ void operator()(const f32x4 (&acc)[2][2][4][2], const Unit& u, int wr, int wc, int fr, int fq) const {
;         const int col0 = u.nt * 128 + wc * 32 + 8 * fq;
; #pragma unroll
;         for (int ai = 0; ai < 2; ++ai)
; #pragma unroll
;             for (int m = 0; m < 4; ++m) { const int rl = ai * 128 + wr * 64 + m * 16 + fr;
.LBB0_960:
	s_nop 15
	s_nop 15
	v_lshl_or_b32 v2, s35, 7, v231
	v_ashrrev_i32_e32 v3, 31, v2
	v_lshl_add_u32 v17, s9, 8, v2
	v_cmp_gt_i32_e32 vcc, s17, v207
	s_and_saveexec_b64 s[4:5], vcc
	s_cbranch_execnz .LBB0_969
	s_or_b64 exec, exec, s[4:5]
	v_cmp_gt_i32_e32 vcc, s17, v224
	s_and_saveexec_b64 s[4:5], vcc
	s_cbranch_execnz .LBB0_970

; __device__ __forceinline__ float fast_exp2(float x) { return __builtin_amdgcn_exp2f(x); }
; __device__ __forceinline__ float fast_rcp(float x) { return __builtin_amdgcn_rcpf(x); }
;     __device__ __forceinline__ void operator()(const f32x4 (&acc)[2][2][4][2], const Unit& u, int wr, int wc, int fr, int fq) const {
;     ...
;             for (int m = 0; m < 4; ++m) { const int rl = ai * 128 + wr * 64 + m * 16 + fr;
;                 f32x4 ov[2];
; #pragma unroll
;                 for (int n = 0; n < 2; ++n) { const f32x4 g = acc[ai][0][m][n], gu = g * acc[ai][1][m][n];
;                     f32x4 d; d.x = fast_exp2(g.x); d.y = fast_exp2(g.y); d.z = fast_exp2(g.z); d.w = fast_exp2(g.w);
;                     d = d + 1.f;
;                     f32x4 r; r.x = fast_rcp(d.x); r.y = fast_rcp(d.y); r.z = fast_rcp(d.z); r.w = fast_rcp(d.w);
;                     ov[n] = gu * r; }
; #pragma unroll
;                 for (int j = 0; j < 4; ++j) { ov[0][j] = __builtin_amdgcn_fmed3f(ov[0][j], -448.f, 448.f); ov[1][j] = __builtin_amdgcn_fmed3f(ov[1][j], -448.f, 448.f); }
;                 int w0 = __builtin_amdgcn_cvt_pk_fp8_f32(ov[0].x, ov[0].y, 0, false); w0 = __builtin_amdgcn_cvt_pk_fp8_f32(ov[0].z, ov[0].w, w0, true);
;                 int w1 = __builtin_amdgcn_cvt_pk_fp8_f32(ov[1].x, ov[1].y, 0, false); w1 = __builtin_amdgcn_cvt_pk_fp8_f32(ov[1].z, ov[1].w, w1, true);
;                 u32x2 w; w.x = (unsigned)w0; w.y = (unsigned)w1;
;                 if (rl < u.nv) *(u32x2*)(act + (size_t)(u.row0 + rl) * EDIM + col0) = w; }
.LBB0_969:
	v_exp_f32_e32 v8, v194
	v_exp_f32_e32 v9, v195
	v_exp_f32_e32 v10, v196
	v_exp_f32_e32 v11, v197
	v_exp_f32_e32 v12, v186
	v_exp_f32_e32 v13, v187
	v_exp_f32_e32 v14, v188
	v_exp_f32_e32 v15, v189
	v_pk_add_f32 v[10:11], v[10:11], 1.0 op_sel_hi:[1,0]
	v_pk_add_f32 v[8:9], v[8:9], 1.0 op_sel_hi:[1,0]
	v_rcp_f32_e32 v10, v10
	v_rcp_f32_e32 v8, v8
	v_rcp_f32_e32 v9, v9
	v_rcp_f32_e32 v11, v11
	v_pk_add_f32 v[14:15], v[14:15], 1.0 op_sel_hi:[1,0]
	v_pk_add_f32 v[12:13], v[12:13], 1.0 op_sel_hi:[1,0]
	v_rcp_f32_e32 v14, v14
	v_rcp_f32_e32 v12, v12
	v_rcp_f32_e32 v13, v13
	v_rcp_f32_e32 v15, v15
	v_pk_mul_f32 v[4:5], v[196:197], v[192:193]
	v_pk_mul_f32 v[6:7], v[194:195], v[190:191]
	v_pk_mul_f32 v[4:5], v[4:5], v[10:11]
	v_pk_mul_f32 v[6:7], v[6:7], v[8:9]
	v_pk_mul_f32 v[8:9], v[188:189], v[184:185]
	v_pk_mul_f32 v[10:11], v[186:187], v[182:183]
	v_pk_mul_f32 v[8:9], v[8:9], v[14:15]
	v_pk_mul_f32 v[10:11], v[10:11], v[12:13]
	v_med3_f32 v16, v5, s22, v235
	v_med3_f32 v5, v9, s22, v235
	v_med3_f32 v9, v4, s22, v235
	v_med3_f32 v11, v11, s22, v235
	v_med3_f32 v10, v10, s22, v235
	v_cvt_pk_fp8_f32 v4, v10, v11
	v_med3_f32 v8, v8, s22, v235
	v_med3_f32 v7, v7, s22, v235
	v_med3_f32 v6, v6, s22, v235
	v_cvt_pk_fp8_f32 v4, v8, v5 op_sel:[0,0,1]
	v_cvt_pk_fp8_f32 v5, v6, v7
	v_lshl_add_u32 v6, v207, 8, v17
	v_cvt_pk_fp8_f32 v5, v9, v16 op_sel:[0,0,1]
	global_store_dwordx2 v6, v[4:5], s[48:49]
	s_or_b64 exec, exec, s[4:5]
	v_cmp_gt_i32_e32 vcc, s17, v224
	s_and_saveexec_b64 s[4:5], vcc
	s_cbranch_execz .LBB0_962
.LBB0_970:
	v_exp_f32_e32 v8, v178
	v_exp_f32_e32 v9, v179
	v_exp_f32_e32 v10, v180
	v_exp_f32_e32 v11, v181
	v_exp_f32_e32 v12, v170
	v_exp_f32_e32 v13, v171
	v_exp_f32_e32 v14, v172
	v_exp_f32_e32 v15, v173
	v_pk_add_f32 v[10:11], v[10:11], 1.0 op_sel_hi:[1,0]
	v_pk_add_f32 v[8:9], v[8:9], 1.0 op_sel_hi:[1,0]
	v_rcp_f32_e32 v10, v10
	v_rcp_f32_e32 v8, v8
	v_rcp_f32_e32 v9, v9
	v_rcp_f32_e32 v11, v11
	v_pk_add_f32 v[14:15], v[14:15], 1.0 op_sel_hi:[1,0]
	v_pk_add_f32 v[12:13], v[12:13], 1.0 op_sel_hi:[1,0]
	v_rcp_f32_e32 v14, v14
	v_rcp_f32_e32 v12, v12
	v_rcp_f32_e32 v13, v13
	v_rcp_f32_e32 v15, v15
	v_pk_mul_f32 v[4:5], v[180:181], v[176:177]
	v_pk_mul_f32 v[6:7], v[178:179], v[174:175]
	v_pk_mul_f32 v[4:5], v[4:5], v[10:11]
	v_pk_mul_f32 v[6:7], v[6:7], v[8:9]
	v_pk_mul_f32 v[8:9], v[172:173], v[168:169]
	v_pk_mul_f32 v[10:11], v[170:171], v[166:167]
	v_pk_mul_f32 v[8:9], v[8:9], v[14:15]
	v_pk_mul_f32 v[10:11], v[10:11], v[12:13]
	v_med3_f32 v16, v5, s22, v235
	v_med3_f32 v5, v9, s22, v235
	v_med3_f32 v9, v4, s22, v235
	v_med3_f32 v11, v11, s22, v235
	v_med3_f32 v10, v10, s22, v235
	v_cvt_pk_fp8_f32 v4, v10, v11
	v_med3_f32 v8, v8, s22, v235
	v_med3_f32 v7, v7, s22, v235
	v_med3_f32 v6, v6, s22, v235
	v_cvt_pk_fp8_f32 v4, v8, v5 op_sel:[0,0,1]
	v_cvt_pk_fp8_f32 v5, v6, v7
	v_lshl_add_u32 v6, v224, 8, v17
	v_cvt_pk_fp8_f32 v5, v9, v16 op_sel:[0,0,1]
	global_store_dwordx2 v6, v[4:5], s[48:49]
	s_or_b64 exec, exec, s[4:5]
	v_cmp_gt_i32_e32 vcc, s17, v225
	s_and_saveexec_b64 s[4:5], vcc
	s_cbranch_execz .LBB0_963
.LBB0_971:
	v_exp_f32_e32 v8, v162
	v_exp_f32_e32 v9, v163
	v_exp_f32_e32 v10, v164
	v_exp_f32_e32 v11, v165
	v_exp_f32_e32 v12, v154
	v_exp_f32_e32 v13, v155
	v_exp_f32_e32 v14, v156
	v_exp_f32_e32 v15, v157
	v_pk_add_f32 v[10:11], v[10:11], 1.0 op_sel_hi:[1,0]
	v_pk_add_f32 v[8:9], v[8:9], 1.0 op_sel_hi:[1,0]
	v_rcp_f32_e32 v10, v10
	v_rcp_f32_e32 v8, v8
	v_rcp_f32_e32 v9, v9
	v_rcp_f32_e32 v11, v11
	v_pk_add_f32 v[14:15], v[14:15], 1.0 op_sel_hi:[1,0]
	v_pk_add_f32 v[12:13], v[12:13], 1.0 op_sel_hi:[1,0]
	v_rcp_f32_e32 v14, v14
	v_rcp_f32_e32 v12, v12
	v_rcp_f32_e32 v13, v13
	v_rcp_f32_e32 v15, v15
	v_pk_mul_f32 v[4:5], v[164:165], v[160:161]
	v_pk_mul_f32 v[6:7], v[162:163], v[158:159]
	v_pk_mul_f32 v[4:5], v[4:5], v[10:11]
	v_pk_mul_f32 v[6:7], v[6:7], v[8:9]
	v_pk_mul_f32 v[8:9], v[156:157], v[152:153]
	v_pk_mul_f32 v[10:11], v[154:155], v[150:151]
	v_pk_mul_f32 v[8:9], v[8:9], v[14:15]
	v_pk_mul_f32 v[10:11], v[10:11], v[12:13]
	v_med3_f32 v16, v5, s22, v235
	v_med3_f32 v5, v9, s22, v235
	v_med3_f32 v9, v4, s22, v235
	v_med3_f32 v11, v11, s22, v235
	v_med3_f32 v10, v10, s22, v235
	v_cvt_pk_fp8_f32 v4, v10, v11
	v_med3_f32 v8, v8, s22, v235
	v_med3_f32 v7, v7, s22, v235
	v_med3_f32 v6, v6, s22, v235
	v_cvt_pk_fp8_f32 v4, v8, v5 op_sel:[0,0,1]
	v_cvt_pk_fp8_f32 v5, v6, v7
	v_lshl_add_u32 v6, v225, 8, v17
	v_cvt_pk_fp8_f32 v5, v9, v16 op_sel:[0,0,1]
	global_store_dwordx2 v6, v[4:5], s[48:49]
	s_or_b64 exec, exec, s[4:5]
	v_cmp_gt_i32_e32 vcc, s17, v226
	s_and_saveexec_b64 s[4:5], vcc
	s_cbranch_execz .LBB0_964
.LBB0_972:
	v_exp_f32_e32 v8, v146
	v_exp_f32_e32 v9, v147
	v_exp_f32_e32 v10, v148
	v_exp_f32_e32 v11, v149
	v_exp_f32_e32 v12, v138
	v_exp_f32_e32 v13, v139
	v_exp_f32_e32 v14, v140
	v_exp_f32_e32 v15, v141
	v_pk_add_f32 v[10:11], v[10:11], 1.0 op_sel_hi:[1,0]
	v_pk_add_f32 v[8:9], v[8:9], 1.0 op_sel_hi:[1,0]
	v_rcp_f32_e32 v10, v10
	v_rcp_f32_e32 v8, v8
	v_rcp_f32_e32 v9, v9
	v_rcp_f32_e32 v11, v11
	v_pk_add_f32 v[14:15], v[14:15], 1.0 op_sel_hi:[1,0]
	v_pk_add_f32 v[12:13], v[12:13], 1.0 op_sel_hi:[1,0]
	v_rcp_f32_e32 v14, v14
	v_rcp_f32_e32 v12, v12
	v_rcp_f32_e32 v13, v13
	v_rcp_f32_e32 v15, v15
	v_pk_mul_f32 v[4:5], v[148:149], v[144:145]
	v_pk_mul_f32 v[6:7], v[146:147], v[142:143]
	v_pk_mul_f32 v[4:5], v[4:5], v[10:11]
	v_pk_mul_f32 v[6:7], v[6:7], v[8:9]
	v_pk_mul_f32 v[8:9], v[140:141], v[136:137]
	v_pk_mul_f32 v[10:11], v[138:139], v[134:135]
	v_pk_mul_f32 v[8:9], v[8:9], v[14:15]
	v_pk_mul_f32 v[10:11], v[10:11], v[12:13]
	v_med3_f32 v16, v5, s22, v235
	v_med3_f32 v5, v9, s22, v235
	v_med3_f32 v9, v4, s22, v235
	v_med3_f32 v11, v11, s22, v235
	v_med3_f32 v10, v10, s22, v235
	v_cvt_pk_fp8_f32 v4, v10, v11
	v_med3_f32 v8, v8, s22, v235
	v_med3_f32 v7, v7, s22, v235
	v_med3_f32 v6, v6, s22, v235
	v_cvt_pk_fp8_f32 v4, v8, v5 op_sel:[0,0,1]
	v_cvt_pk_fp8_f32 v5, v6, v7
	v_lshl_add_u32 v6, v226, 8, v17
	v_cvt_pk_fp8_f32 v5, v9, v16 op_sel:[0,0,1]
	global_store_dwordx2 v6, v[4:5], s[48:49]
	s_or_b64 exec, exec, s[4:5]
	v_cmp_gt_i32_e32 vcc, s17, v227
	s_and_saveexec_b64 s[4:5], vcc
	s_cbranch_execz .LBB0_965
; __device__ __forceinline__ float fast_exp2(float x) { return __builtin_amdgcn_exp2f(x); }
; __device__ __forceinline__ float fast_rcp(float x) { return __builtin_amdgcn_rcpf(x); }
;     __device__ __forceinline__ void operator()(const f32x4 (&acc)[2][2][4][2], const Unit& u, int wr, int wc, int fr, int fq) const {
;     ...
;             for (int m = 0; m < 4; ++m) { const int rl = ai * 128 + wr * 64 + m * 16 + fr;
;                 f32x4 ov[2];
; #pragma unroll
;                 for (int n = 0; n < 2; ++n) { const f32x4 g = acc[ai][0][m][n], gu = g * acc[ai][1][m][n];
;                     f32x4 d; d.x = fast_exp2(g.x); d.y = fast_exp2(g.y); d.z = fast_exp2(g.z); d.w = fast_exp2(g.w);
;                     d = d + 1.f;
;                     f32x4 r; r.x = fast_rcp(d.x); r.y = fast_rcp(d.y); r.z = fast_rcp(d.z); r.w = fast_rcp(d.w);
;                     ov[n] = gu * r; }
; #pragma unroll
;                 for (int j = 0; j < 4; ++j) { ov[0][j] = __builtin_amdgcn_fmed3f(ov[0][j], -448.f, 448.f); ov[1][j] = __builtin_amdgcn_fmed3f(ov[1][j], -448.f, 448.f); }
;                 int w0 = __builtin_amdgcn_cvt_pk_fp8_f32(ov[0].x, ov[0].y, 0, false); w0 = __builtin_amdgcn_cvt_pk_fp8_f32(ov[0].z, ov[0].w, w0, true);
;                 int w1 = __builtin_amdgcn_cvt_pk_fp8_f32(ov[1].x, ov[1].y, 0, false); w1 = __builtin_amdgcn_cvt_pk_fp8_f32(ov[1].z, ov[1].w, w1, true);
;                 u32x2 w; w.x = (unsigned)w0; w.y = (unsigned)w1;
;                 if (rl < u.nv) *(u32x2*)(act + (size_t)(u.row0 + rl) * EDIM + col0) = w; }
.LBB0_973:
	v_exp_f32_e32 v8, v126
	v_exp_f32_e32 v9, v127
	v_exp_f32_e32 v10, v128
	v_exp_f32_e32 v11, v129
	v_exp_f32_e32 v12, v118
	v_exp_f32_e32 v13, v119
	v_exp_f32_e32 v14, v120
	v_exp_f32_e32 v15, v121
	v_pk_add_f32 v[10:11], v[10:11], 1.0 op_sel_hi:[1,0]
	v_pk_add_f32 v[8:9], v[8:9], 1.0 op_sel_hi:[1,0]
	v_rcp_f32_e32 v10, v10
	v_rcp_f32_e32 v8, v8
	v_rcp_f32_e32 v9, v9
	v_rcp_f32_e32 v11, v11
	v_pk_add_f32 v[14:15], v[14:15], 1.0 op_sel_hi:[1,0]
	v_pk_add_f32 v[12:13], v[12:13], 1.0 op_sel_hi:[1,0]
	v_rcp_f32_e32 v14, v14
	v_rcp_f32_e32 v12, v12
	v_rcp_f32_e32 v13, v13
	v_rcp_f32_e32 v15, v15
	v_pk_mul_f32 v[4:5], v[132:133], v[128:129]
	v_pk_mul_f32 v[6:7], v[130:131], v[126:127]
	v_pk_mul_f32 v[4:5], v[4:5], v[10:11]
	v_pk_mul_f32 v[6:7], v[6:7], v[8:9]
	v_pk_mul_f32 v[8:9], v[124:125], v[120:121]
	v_pk_mul_f32 v[10:11], v[122:123], v[118:119]
	v_pk_mul_f32 v[8:9], v[8:9], v[14:15]
	v_pk_mul_f32 v[10:11], v[10:11], v[12:13]
	v_med3_f32 v16, v5, s22, v235
	v_med3_f32 v5, v9, s22, v235
	v_med3_f32 v9, v4, s22, v235
	v_med3_f32 v11, v11, s22, v235
	v_med3_f32 v10, v10, s22, v235
	v_cvt_pk_fp8_f32 v4, v10, v11
	v_med3_f32 v8, v8, s22, v235
	v_med3_f32 v7, v7, s22, v235
	v_med3_f32 v6, v6, s22, v235
	v_cvt_pk_fp8_f32 v4, v8, v5 op_sel:[0,0,1]
	v_cvt_pk_fp8_f32 v5, v6, v7
	v_lshl_add_u32 v6, v227, 8, v17
	v_cvt_pk_fp8_f32 v5, v9, v16 op_sel:[0,0,1]
	global_store_dwordx2 v6, v[4:5], s[48:49]
	s_or_b64 exec, exec, s[4:5]
	v_cmp_gt_i32_e32 vcc, s17, v228
	s_and_saveexec_b64 s[4:5], vcc
	s_cbranch_execz .LBB0_966
.LBB0_974:
	v_exp_f32_e32 v8, v110
	v_exp_f32_e32 v9, v111
	v_exp_f32_e32 v10, v112
	v_exp_f32_e32 v11, v113
	v_exp_f32_e32 v12, v102
	v_exp_f32_e32 v13, v103
	v_exp_f32_e32 v14, v104
	v_exp_f32_e32 v15, v105
	v_pk_add_f32 v[10:11], v[10:11], 1.0 op_sel_hi:[1,0]
	v_pk_add_f32 v[8:9], v[8:9], 1.0 op_sel_hi:[1,0]
	v_rcp_f32_e32 v10, v10
	v_rcp_f32_e32 v8, v8
	v_rcp_f32_e32 v9, v9
	v_rcp_f32_e32 v11, v11
	v_pk_add_f32 v[14:15], v[14:15], 1.0 op_sel_hi:[1,0]
	v_pk_add_f32 v[12:13], v[12:13], 1.0 op_sel_hi:[1,0]
	v_rcp_f32_e32 v14, v14
	v_rcp_f32_e32 v12, v12
	v_rcp_f32_e32 v13, v13
	v_rcp_f32_e32 v15, v15
	v_pk_mul_f32 v[4:5], v[116:117], v[112:113]
	v_pk_mul_f32 v[6:7], v[114:115], v[110:111]
	v_pk_mul_f32 v[4:5], v[4:5], v[10:11]
	v_pk_mul_f32 v[6:7], v[6:7], v[8:9]
	v_pk_mul_f32 v[8:9], v[108:109], v[104:105]
	v_pk_mul_f32 v[10:11], v[106:107], v[102:103]
	v_pk_mul_f32 v[8:9], v[8:9], v[14:15]
	v_pk_mul_f32 v[10:11], v[10:11], v[12:13]
	v_med3_f32 v16, v5, s22, v235
	v_med3_f32 v5, v9, s22, v235
	v_med3_f32 v9, v4, s22, v235
	v_med3_f32 v11, v11, s22, v235
	v_med3_f32 v10, v10, s22, v235
	v_cvt_pk_fp8_f32 v4, v10, v11
	v_med3_f32 v8, v8, s22, v235
	v_med3_f32 v7, v7, s22, v235
	v_med3_f32 v6, v6, s22, v235
	v_cvt_pk_fp8_f32 v4, v8, v5 op_sel:[0,0,1]
	v_cvt_pk_fp8_f32 v5, v6, v7
	v_lshl_add_u32 v6, v228, 8, v17
	v_cvt_pk_fp8_f32 v5, v9, v16 op_sel:[0,0,1]
	global_store_dwordx2 v6, v[4:5], s[48:49]
	s_or_b64 exec, exec, s[4:5]
	v_cmp_gt_i32_e32 vcc, s17, v229
	s_and_saveexec_b64 s[4:5], vcc
	s_cbranch_execz .LBB0_967
.LBB0_975:
	v_exp_f32_e32 v8, v94
	v_exp_f32_e32 v9, v95
	v_exp_f32_e32 v10, v96
	v_exp_f32_e32 v11, v97
	v_exp_f32_e32 v12, v86
	v_exp_f32_e32 v13, v87
	v_exp_f32_e32 v14, v88
	v_exp_f32_e32 v15, v89
	v_pk_add_f32 v[10:11], v[10:11], 1.0 op_sel_hi:[1,0]
	v_pk_add_f32 v[8:9], v[8:9], 1.0 op_sel_hi:[1,0]
	v_rcp_f32_e32 v10, v10
	v_rcp_f32_e32 v8, v8
	v_rcp_f32_e32 v9, v9
	v_rcp_f32_e32 v11, v11
	v_pk_add_f32 v[14:15], v[14:15], 1.0 op_sel_hi:[1,0]
	v_pk_add_f32 v[12:13], v[12:13], 1.0 op_sel_hi:[1,0]
	v_rcp_f32_e32 v14, v14
	v_rcp_f32_e32 v12, v12
	v_rcp_f32_e32 v13, v13
	v_rcp_f32_e32 v15, v15
	v_pk_mul_f32 v[4:5], v[96:97], v[100:101]
	v_pk_mul_f32 v[6:7], v[94:95], v[98:99]
	v_pk_mul_f32 v[4:5], v[4:5], v[10:11]
	v_pk_mul_f32 v[6:7], v[6:7], v[8:9]
	v_pk_mul_f32 v[8:9], v[88:89], v[92:93]
	v_pk_mul_f32 v[10:11], v[86:87], v[90:91]
	v_pk_mul_f32 v[8:9], v[8:9], v[14:15]
	v_pk_mul_f32 v[10:11], v[10:11], v[12:13]
	v_med3_f32 v16, v5, s22, v235
	v_med3_f32 v5, v9, s22, v235
	v_med3_f32 v9, v4, s22, v235
	v_med3_f32 v11, v11, s22, v235
	v_med3_f32 v10, v10, s22, v235
	v_cvt_pk_fp8_f32 v4, v10, v11
	v_med3_f32 v8, v8, s22, v235
	v_med3_f32 v7, v7, s22, v235
	v_med3_f32 v6, v6, s22, v235
	v_cvt_pk_fp8_f32 v4, v8, v5 op_sel:[0,0,1]
	v_cvt_pk_fp8_f32 v5, v6, v7
	v_lshl_add_u32 v6, v229, 8, v17
	v_cvt_pk_fp8_f32 v5, v9, v16 op_sel:[0,0,1]
	global_store_dwordx2 v6, v[4:5], s[48:49]
	s_or_b64 exec, exec, s[4:5]
	v_cmp_gt_i32_e32 vcc, s17, v230
	s_and_saveexec_b64 s[4:5], vcc
	s_cbranch_execz .LBB0_968
.LBB0_976:
	v_exp_f32_e32 v8, v78
	v_exp_f32_e32 v9, v79
	v_exp_f32_e32 v10, v80
	v_exp_f32_e32 v11, v81
	v_exp_f32_e32 v12, v70
	v_exp_f32_e32 v13, v71
	v_exp_f32_e32 v14, v72
	v_exp_f32_e32 v15, v73
	v_pk_add_f32 v[10:11], v[10:11], 1.0 op_sel_hi:[1,0]
	v_pk_add_f32 v[8:9], v[8:9], 1.0 op_sel_hi:[1,0]
	v_rcp_f32_e32 v10, v10
	v_rcp_f32_e32 v8, v8
	v_rcp_f32_e32 v9, v9
	v_rcp_f32_e32 v11, v11
	v_pk_add_f32 v[14:15], v[14:15], 1.0 op_sel_hi:[1,0]
	v_pk_add_f32 v[12:13], v[12:13], 1.0 op_sel_hi:[1,0]
	v_rcp_f32_e32 v14, v14
	v_rcp_f32_e32 v12, v12
	v_rcp_f32_e32 v13, v13
	v_rcp_f32_e32 v15, v15
	v_pk_mul_f32 v[4:5], v[80:81], v[84:85]
	v_pk_mul_f32 v[6:7], v[78:79], v[82:83]
	v_pk_mul_f32 v[4:5], v[4:5], v[10:11]
	v_pk_mul_f32 v[6:7], v[6:7], v[8:9]
	v_pk_mul_f32 v[8:9], v[72:73], v[76:77]
	v_pk_mul_f32 v[10:11], v[70:71], v[74:75]
	v_pk_mul_f32 v[8:9], v[8:9], v[14:15]
	v_pk_mul_f32 v[10:11], v[10:11], v[12:13]
	v_med3_f32 v16, v5, s22, v235
	v_med3_f32 v5, v9, s22, v235
	v_med3_f32 v9, v4, s22, v235
	v_med3_f32 v11, v11, s22, v235
	v_med3_f32 v10, v10, s22, v235
	v_cvt_pk_fp8_f32 v4, v10, v11
	v_med3_f32 v8, v8, s22, v235
	v_med3_f32 v7, v7, s22, v235
	v_med3_f32 v6, v6, s22, v235
	v_cvt_pk_fp8_f32 v4, v8, v5 op_sel:[0,0,1]
	v_cvt_pk_fp8_f32 v5, v6, v7
	v_lshl_add_u32 v6, v230, 8, v17
	v_cvt_pk_fp8_f32 v5, v9, v16 op_sel:[0,0,1]
	global_store_dwordx2 v6, v[4:5], s[48:49]
	s_or_b64 exec, exec, s[4:5]
	s_cmp_lg_u32 s34, s21
	s_mov_b64 s[4:5], -1
	s_cbranch_scc0 .LBB0_947
